# P4 pipelined loop waits with vmcnt(6): previous iteration's store left outstanding (first iteration peeled)
# speedup vs baseline: 1.0836x; 1.0067x over previous
; __device__ __forceinline__ unsigned pk2(float lo, float hi) { return f2bf(lo) | (f2bf(hi) << 16); }
; __device__ __forceinline__ float siluf_(float x) { return x * __builtin_amdgcn_rcpf(1.0f + __expf(-x)); }
; __device__ __forceinline__ void gdn_gate_norm(const Params& P, size_t wi, size_t nw) {
;     ...
;     for (size_t i = wi; i < (size_t)T * 64; i += nw) {
;         const size_t t = i >> 6; const int c0 = (int)(i & 63) * 8, h = c0 >> 7;
;         const f32x4 q0 = *(const f32x4*)(SSQG + t * 32 + h * 8);
;         const float rstd = rsqrtf(((q0.x + q0.y) + (q0.z + q0.w)) * (1.0f / 128.0f) + 1e-6f);
;         const v4u o = *(const v4u*)(Y + t * 1024 + c0), z = Z[i];
;         const f32x4 w0 = *(const f32x4*)(P.gdn_norm_w + (c0 & 127)), w1 = *(const f32x4*)(P.gdn_norm_w + (c0 & 127) + 4);
;         float y[8];
;         y[0] = bflo(o.x) * rstd * w0.x * siluf_(bflo(z.x)); y[1] = bfhi(o.x) * rstd * w0.y * siluf_(bfhi(z.x));
;         y[2] = bflo(o.y) * rstd * w0.z * siluf_(bflo(z.y)); y[3] = bfhi(o.y) * rstd * w0.w * siluf_(bfhi(z.y));
;         y[4] = bflo(o.z) * rstd * w1.x * siluf_(bflo(z.z)); y[5] = bfhi(o.z) * rstd * w1.y * siluf_(bfhi(z.z));
;         y[6] = bflo(o.w) * rstd * w1.z * siluf_(bflo(z.w)); y[7] = bfhi(o.w) * rstd * w1.w * siluf_(bfhi(z.w));
;         v4u r; r.x = pk2(y[0], y[1]); r.y = pk2(y[2], y[3]); r.z = pk2(y[4], y[5]); r.w = pk2(y[6], y[7]);
;         *(v4u*)(Y + t * 1024 + c0) = r;
;     }
.LBB0_2269:
	s_cmp_lt_i32 s74, 5
	s_cselect_b64 s[4:5], -1, 0
	s_and_b64 s[4:5], s[4:5], s[0:1]
	s_andn2_b64 vcc, exec, s[4:5]
	s_cbranch_vccnz .LBB0_2274
	s_ashr_i32 s3, s2, 31
	s_lshl_b64 s[0:1], s[2:3], 9
	v_or_b32_e32 v2, s0, v0
	v_mov_b32_e32 v3, s1
	s_mov_b64 s[0:1], 0x100000
	v_cmp_gt_u64_e32 vcc, s[0:1], v[2:3]
	s_and_saveexec_b64 s[0:1], vcc
	v_readlane_b32 s8, v254, 4
	v_readlane_b32 s22, v254, 18
	v_readlane_b32 s23, v254, 19
	v_readlane_b32 s9, v254, 5
	v_readlane_b32 s10, v254, 6
	v_readlane_b32 s11, v254, 7
	v_readlane_b32 s12, v254, 8
	v_readlane_b32 s13, v254, 9
	v_readlane_b32 s14, v254, 10
	v_readlane_b32 s15, v254, 11
	v_readlane_b32 s16, v254, 12
	v_readlane_b32 s17, v254, 13
	v_readlane_b32 s18, v254, 14
	v_readlane_b32 s19, v254, 15
	v_readlane_b32 s20, v254, 16
	v_readlane_b32 s21, v254, 17
	s_cbranch_execz .LBB0_2273
	s_ashr_i32 s27, s26, 31
	s_lshl_b64 s[6:7], s[26:27], 9
	s_add_u32 s8, s94, 0x400000
	s_addc_u32 s9, s95, 0
	s_lshl_b64 s[10:11], s[2:3], 13
	s_add_u32 s10, s24, s10
	v_mov_b32_e32 v5, 0
	v_lshlrev_b32_e32 v4, 4, v0
	s_addc_u32 s11, s25, s11
	v_lshl_add_u64 v[6:7], s[10:11], 0, v[4:5]
	s_mov_b64 s[10:11], 0x7c00000
	v_lshlrev_b32_e32 v1, 3, v0
	v_lshl_add_u64 v[6:7], v[6:7], 0, s[10:11]
	s_lshl_b64 s[10:11], s[26:27], 13
	v_lshl_or_b32 v1, s2, 12, v1
	s_lshl_b32 s3, s26, 12
	s_mov_b64 s[12:13], 0
	v_mov_b32_e32 v8, 0x358637bd
	s_mov_b32 s16, 0x800000
	s_mov_b32 s17, 0xffff0000
	s_movk_i32 s18, 0x7fff
	s_mov_b64 s[14:15], 0xfffff
	v_mov_b32_e32 v87, 0
	v_lshrrev_b64 v[14:15], 6, v[2:3]
	global_load_dwordx4 v[10:13], v[6:7], off
	v_lshlrev_b32_e32 v4, 1, v2
	v_lshlrev_b64 v[22:23], 7, v[14:15]
	v_and_b32_e32 v16, 0x78, v1
	v_and_b32_e32 v4, 0x60, v4
	v_lshl_add_u64 v[22:23], s[94:95], 0, v[22:23]
	v_lshlrev_b64 v[24:25], 11, v[14:15]
	v_lshlrev_b32_e32 v26, 2, v16
	v_lshl_add_u64 v[22:23], v[22:23], 0, v[4:5]
	global_load_dwordx4 v[14:17], v26, s[22:23]
	global_load_dwordx4 v[18:21], v26, s[22:23] offset:16
	v_lshl_add_u64 v[26:27], s[8:9], 0, v[24:25]
	global_load_dwordx4 v[22:25], v[22:23], off
	v_and_b32_e32 v9, 0x1f8, v1
	v_lshlrev_b32_e32 v4, 1, v9
	v_lshl_add_u64 v[30:31], v[26:27], 0, v[4:5]
	global_load_dwordx4 v[26:29], v[30:31], off
	v_lshl_add_u64 v[2:3], v[2:3], 0, s[6:7]
	v_cmp_lt_u64_e32 vcc, s[14:15], v[2:3]
	s_or_b64 s[12:13], vcc, s[12:13]
	v_lshl_add_u64 v[6:7], v[6:7], 0, s[10:11]
	v_add_u32_e32 v1, s3, v1
	s_mov_b64 s[98:99], exec
	s_andn2_b64 exec, exec, s[12:13]
	s_cbranch_execz .Lp4_lastA
	v_lshrrev_b64 v[54:55], 6, v[2:3]
	global_load_dwordx4 v[50:53], v[6:7], off
	v_lshlrev_b32_e32 v86, 1, v2
	v_lshlrev_b64 v[62:63], 7, v[54:55]
	v_and_b32_e32 v56, 0x78, v1
	v_and_b32_e32 v86, 0x60, v86
	v_lshl_add_u64 v[62:63], s[94:95], 0, v[62:63]
	v_lshlrev_b64 v[64:65], 11, v[54:55]
	v_lshlrev_b32_e32 v66, 2, v56
	v_lshl_add_u64 v[62:63], v[62:63], 0, v[86:87]
	global_load_dwordx4 v[54:57], v66, s[22:23]
	global_load_dwordx4 v[58:61], v66, s[22:23] offset:16
	v_lshl_add_u64 v[66:67], s[8:9], 0, v[64:65]
	global_load_dwordx4 v[62:65], v[62:63], off
	v_and_b32_e32 v88, 0x1f8, v1
	v_lshlrev_b32_e32 v86, 1, v88
	v_lshl_add_u64 v[70:71], v[66:67], 0, v[86:87]
	global_load_dwordx4 v[66:69], v[70:71], off
	v_lshl_add_u64 v[2:3], v[2:3], 0, s[6:7]
	v_cmp_lt_u64_e32 vcc, s[14:15], v[2:3]
	s_or_b64 s[12:13], vcc, s[12:13]
	v_lshl_add_u64 v[6:7], v[6:7], 0, s[10:11]
	v_add_u32_e32 v1, s3, v1
	s_mov_b64 s[100:101], exec
	s_mov_b64 exec, s[98:99]
	s_waitcnt vmcnt(5)
	v_lshlrev_b32_e32 v32, 16, v10
	v_mul_f32_e32 v4, 0xbfb8aa3b, v32
	v_exp_f32_e32 v4, v4
	v_lshlrev_b32_e32 v33, 16, v11
	v_lshlrev_b32_e32 v35, 16, v13
	v_lshlrev_b32_e32 v34, 16, v12
	v_and_b32_e32 v13, 0xffff0000, v13
	v_and_b32_e32 v12, 0xffff0000, v12
	v_mov_b32_e32 v36, v14
	v_mov_b32_e32 v37, v16
	v_mov_b32_e32 v16, v15
	v_mov_b32_e32 v14, v18
	v_mov_b32_e32 v15, v20
	v_mov_b32_e32 v20, v19
	v_mov_b32_e32 v18, v23
	v_mov_b32_e32 v19, v24
	v_mov_b32_e32 v23, v25
	v_pk_add_f32 v[18:19], v[18:19], v[22:23]
	v_and_b32_e32 v11, 0xffff0000, v11
	v_add_f32_e32 v18, v18, v19
	v_and_b32_e32 v10, 0xffff0000, v10
	v_mul_f32_e32 v38, 0xbfb8aa3b, v33
	v_mul_f32_e32 v40, 0xbfb8aa3b, v34
	v_mul_f32_e32 v41, 0xbfb8aa3b, v12
	v_mul_f32_e32 v42, 0xbfb8aa3b, v35
	v_mul_f32_e32 v43, 0xbfb8aa3b, v13
	v_add_f32_e32 v4, 1.0, v4
	v_fmamk_f32 v45, v18, 0x3c000000, v8
	v_mul_f32_e32 v9, 0xbfb8aa3b, v10
	v_mul_f32_e32 v39, 0xbfb8aa3b, v11
	v_exp_f32_e32 v38, v38
	v_exp_f32_e32 v40, v40
	v_exp_f32_e32 v41, v41
	v_exp_f32_e32 v42, v42
	v_exp_f32_e32 v43, v43
	v_rcp_f32_e32 v18, v4
	v_mul_f32_e32 v4, 0x4b800000, v45
	v_cmp_gt_f32_e32 vcc, s16, v45
	v_exp_f32_e32 v9, v9
	v_exp_f32_e32 v39, v39
	v_cndmask_b32_e32 v4, v45, v4, vcc
	v_rsq_f32_e32 v4, v4
	v_add_f32_e32 v19, 1.0, v38
	v_add_f32_e32 v40, 1.0, v40
	v_add_f32_e32 v41, 1.0, v41
	v_add_f32_e32 v44, 1.0, v42
	v_add_f32_e32 v43, 1.0, v43
	v_add_f32_e32 v9, 1.0, v9
	v_add_f32_e32 v39, 1.0, v39
	v_rcp_f32_e32 v19, v19
	v_rcp_f32_e32 v40, v40
	v_rcp_f32_e32 v42, v41
	v_rcp_f32_e32 v41, v44
	v_rcp_f32_e32 v43, v43
	v_rcp_f32_e32 v38, v9
	v_rcp_f32_e32 v39, v39
	v_mul_f32_e32 v9, 0x45800000, v4
	v_lshlrev_b32_e32 v23, 16, v27
	v_lshlrev_b32_e32 v22, 16, v26
	v_and_b32_e32 v25, 0xffff0000, v27
	v_and_b32_e32 v24, 0xffff0000, v26
	v_lshlrev_b32_e32 v27, 16, v29
	v_lshlrev_b32_e32 v26, 16, v28
	v_and_b32_e32 v29, 0xffff0000, v29
	v_and_b32_e32 v28, 0xffff0000, v28
	v_cndmask_b32_e32 v4, v4, v9, vcc
	v_pk_mul_f32 v[22:23], v[4:5], v[22:23] op_sel_hi:[0,1]
	v_pk_mul_f32 v[26:27], v[4:5], v[26:27] op_sel_hi:[0,1]
	v_pk_mul_f32 v[28:29], v[4:5], v[28:29] op_sel_hi:[0,1]
	v_pk_mul_f32 v[18:19], v[18:19], v[32:33]
	v_pk_mul_f32 v[32:33], v[40:41], v[34:35]
	v_pk_mul_f32 v[12:13], v[42:43], v[12:13]
	v_pk_mul_f32 v[24:25], v[4:5], v[24:25] op_sel_hi:[0,1]
	v_pk_mul_f32 v[22:23], v[36:37], v[22:23]
	v_pk_mul_f32 v[14:15], v[14:15], v[26:27]
	v_pk_mul_f32 v[20:21], v[20:21], v[28:29]
	v_pk_mul_f32 v[10:11], v[38:39], v[10:11]
	v_pk_mul_f32 v[16:17], v[16:17], v[24:25]
	v_pk_mul_f32 v[18:19], v[18:19], v[22:23]
	v_pk_mul_f32 v[14:15], v[32:33], v[14:15]
	v_pk_mul_f32 v[12:13], v[12:13], v[20:21]
	v_pk_mul_f32 v[10:11], v[10:11], v[16:17]
	v_cvt_pk_bf16_f32 v10, v18, v10
	v_cvt_pk_bf16_f32 v11, v19, v11
	v_cvt_pk_bf16_f32 v12, v14, v12
	v_cvt_pk_bf16_f32 v13, v15, v13
	global_store_dwordx4 v[30:31], v[10:13], off
	s_mov_b64 exec, s[100:101]
; __device__ __forceinline__ unsigned pk2(float lo, float hi) { return f2bf(lo) | (f2bf(hi) << 16); }
; __device__ __forceinline__ float siluf_(float x) { return x * __builtin_amdgcn_rcpf(1.0f + __expf(-x)); }
; __device__ __forceinline__ void gdn_gate_norm(const Params& P, size_t wi, size_t nw) {
;     ...
;     for (size_t i = wi; i < (size_t)T * 64; i += nw) {
;         const size_t t = i >> 6; const int c0 = (int)(i & 63) * 8, h = c0 >> 7;
;         const f32x4 q0 = *(const f32x4*)(SSQG + t * 32 + h * 8);
;         const float rstd = rsqrtf(((q0.x + q0.y) + (q0.z + q0.w)) * (1.0f / 128.0f) + 1e-6f);
;         const v4u o = *(const v4u*)(Y + t * 1024 + c0), z = Z[i];
;         const f32x4 w0 = *(const f32x4*)(P.gdn_norm_w + (c0 & 127)), w1 = *(const f32x4*)(P.gdn_norm_w + (c0 & 127) + 4);
;         float y[8];
;         y[0] = bflo(o.x) * rstd * w0.x * siluf_(bflo(z.x)); y[1] = bfhi(o.x) * rstd * w0.y * siluf_(bfhi(z.x));
;         y[2] = bflo(o.y) * rstd * w0.z * siluf_(bflo(z.y)); y[3] = bfhi(o.y) * rstd * w0.w * siluf_(bfhi(z.y));
;         y[4] = bflo(o.z) * rstd * w1.x * siluf_(bflo(z.z)); y[5] = bfhi(o.z) * rstd * w1.y * siluf_(bfhi(z.z));
;         y[6] = bflo(o.w) * rstd * w1.z * siluf_(bflo(z.w)); y[7] = bfhi(o.w) * rstd * w1.w * siluf_(bfhi(z.w));
;         v4u r; r.x = pk2(y[0], y[1]); r.y = pk2(y[2], y[3]); r.z = pk2(y[4], y[5]); r.w = pk2(y[6], y[7]);
;         *(v4u*)(Y + t * 1024 + c0) = r;
.Lp4_loop:
	s_mov_b64 s[98:99], exec
	s_andn2_b64 exec, exec, s[12:13]
	s_cbranch_execz .Lp4_lastB
	v_lshrrev_b64 v[14:15], 6, v[2:3]
	global_load_dwordx4 v[10:13], v[6:7], off
	v_lshlrev_b32_e32 v4, 1, v2
	v_lshlrev_b64 v[22:23], 7, v[14:15]
	v_and_b32_e32 v16, 0x78, v1
	v_and_b32_e32 v4, 0x60, v4
	v_lshl_add_u64 v[22:23], s[94:95], 0, v[22:23]
	v_lshlrev_b64 v[24:25], 11, v[14:15]
	v_lshlrev_b32_e32 v26, 2, v16
	v_lshl_add_u64 v[22:23], v[22:23], 0, v[4:5]
	global_load_dwordx4 v[14:17], v26, s[22:23]
	global_load_dwordx4 v[18:21], v26, s[22:23] offset:16
	v_lshl_add_u64 v[26:27], s[8:9], 0, v[24:25]
	global_load_dwordx4 v[22:25], v[22:23], off
	v_and_b32_e32 v9, 0x1f8, v1
	v_lshlrev_b32_e32 v4, 1, v9
	v_lshl_add_u64 v[30:31], v[26:27], 0, v[4:5]
	global_load_dwordx4 v[26:29], v[30:31], off
	v_lshl_add_u64 v[2:3], v[2:3], 0, s[6:7]
	v_cmp_lt_u64_e32 vcc, s[14:15], v[2:3]
	s_or_b64 s[12:13], vcc, s[12:13]
	v_lshl_add_u64 v[6:7], v[6:7], 0, s[10:11]
	v_add_u32_e32 v1, s3, v1
	s_mov_b64 s[100:101], exec
	s_mov_b64 exec, s[98:99]
	s_waitcnt vmcnt(6)
	v_lshlrev_b32_e32 v72, 16, v50
	v_mul_f32_e32 v86, 0xbfb8aa3b, v72
	v_exp_f32_e32 v86, v86
	v_lshlrev_b32_e32 v73, 16, v51
	v_lshlrev_b32_e32 v75, 16, v53
	v_lshlrev_b32_e32 v74, 16, v52
	v_and_b32_e32 v53, 0xffff0000, v53
	v_and_b32_e32 v52, 0xffff0000, v52
	v_mov_b32_e32 v76, v54
	v_mov_b32_e32 v77, v56
	v_mov_b32_e32 v56, v55
	v_mov_b32_e32 v54, v58
	v_mov_b32_e32 v55, v60
	v_mov_b32_e32 v60, v59
	v_mov_b32_e32 v58, v63
	v_mov_b32_e32 v59, v64
	v_mov_b32_e32 v63, v65
	v_pk_add_f32 v[58:59], v[58:59], v[62:63]
	v_and_b32_e32 v51, 0xffff0000, v51
	v_add_f32_e32 v58, v58, v59
	v_and_b32_e32 v50, 0xffff0000, v50
	v_mul_f32_e32 v78, 0xbfb8aa3b, v73
	v_mul_f32_e32 v80, 0xbfb8aa3b, v74
	v_mul_f32_e32 v81, 0xbfb8aa3b, v52
	v_mul_f32_e32 v82, 0xbfb8aa3b, v75
	v_mul_f32_e32 v83, 0xbfb8aa3b, v53
	v_add_f32_e32 v86, 1.0, v86
	v_fmamk_f32 v85, v58, 0x3c000000, v8
	v_mul_f32_e32 v88, 0xbfb8aa3b, v50
	v_mul_f32_e32 v79, 0xbfb8aa3b, v51
	v_exp_f32_e32 v78, v78
	v_exp_f32_e32 v80, v80
	v_exp_f32_e32 v81, v81
	v_exp_f32_e32 v82, v82
	v_exp_f32_e32 v83, v83
	v_rcp_f32_e32 v58, v86
	v_mul_f32_e32 v86, 0x4b800000, v85
	v_cmp_gt_f32_e32 vcc, s16, v85
	v_exp_f32_e32 v88, v88
	v_exp_f32_e32 v79, v79
	v_cndmask_b32_e32 v86, v85, v86, vcc
	v_rsq_f32_e32 v86, v86
	v_add_f32_e32 v59, 1.0, v78
	v_add_f32_e32 v80, 1.0, v80
	v_add_f32_e32 v81, 1.0, v81
	v_add_f32_e32 v84, 1.0, v82
	v_add_f32_e32 v83, 1.0, v83
	v_add_f32_e32 v88, 1.0, v88
	v_add_f32_e32 v79, 1.0, v79
	v_rcp_f32_e32 v59, v59
	v_rcp_f32_e32 v80, v80
	v_rcp_f32_e32 v82, v81
	v_rcp_f32_e32 v81, v84
	v_rcp_f32_e32 v83, v83
	v_rcp_f32_e32 v78, v88
	v_rcp_f32_e32 v79, v79
	v_mul_f32_e32 v88, 0x45800000, v86
	v_lshlrev_b32_e32 v63, 16, v67
	v_lshlrev_b32_e32 v62, 16, v66
	v_and_b32_e32 v65, 0xffff0000, v67
	v_and_b32_e32 v64, 0xffff0000, v66
	v_lshlrev_b32_e32 v67, 16, v69
	v_lshlrev_b32_e32 v66, 16, v68
	v_and_b32_e32 v69, 0xffff0000, v69
	v_and_b32_e32 v68, 0xffff0000, v68
	v_cndmask_b32_e32 v86, v86, v88, vcc
	v_pk_mul_f32 v[62:63], v[86:87], v[62:63] op_sel_hi:[0,1]
	v_pk_mul_f32 v[66:67], v[86:87], v[66:67] op_sel_hi:[0,1]
	v_pk_mul_f32 v[68:69], v[86:87], v[68:69] op_sel_hi:[0,1]
	v_pk_mul_f32 v[58:59], v[58:59], v[72:73]
	v_pk_mul_f32 v[72:73], v[80:81], v[74:75]
	v_pk_mul_f32 v[52:53], v[82:83], v[52:53]
	v_pk_mul_f32 v[64:65], v[86:87], v[64:65] op_sel_hi:[0,1]
	v_pk_mul_f32 v[62:63], v[76:77], v[62:63]
	v_pk_mul_f32 v[54:55], v[54:55], v[66:67]
	v_pk_mul_f32 v[60:61], v[60:61], v[68:69]
	v_pk_mul_f32 v[50:51], v[78:79], v[50:51]
	v_pk_mul_f32 v[56:57], v[56:57], v[64:65]
	v_pk_mul_f32 v[58:59], v[58:59], v[62:63]
	v_pk_mul_f32 v[54:55], v[72:73], v[54:55]
	v_pk_mul_f32 v[52:53], v[52:53], v[60:61]
	v_pk_mul_f32 v[50:51], v[50:51], v[56:57]
	v_cvt_pk_bf16_f32 v50, v58, v50
	v_cvt_pk_bf16_f32 v51, v59, v51
	v_cvt_pk_bf16_f32 v52, v54, v52
	v_cvt_pk_bf16_f32 v53, v55, v53
	global_store_dwordx4 v[70:71], v[50:53], off
	s_mov_b64 exec, s[100:101]
	s_mov_b64 s[98:99], exec
	s_andn2_b64 exec, exec, s[12:13]
	s_cbranch_execz .Lp4_lastA
; __device__ __forceinline__ unsigned pk2(float lo, float hi) { return f2bf(lo) | (f2bf(hi) << 16); }
; __device__ __forceinline__ float siluf_(float x) { return x * __builtin_amdgcn_rcpf(1.0f + __expf(-x)); }
; __device__ __forceinline__ void gdn_gate_norm(const Params& P, size_t wi, size_t nw) {
;     ...
;     for (size_t i = wi; i < (size_t)T * 64; i += nw) {
;         const size_t t = i >> 6; const int c0 = (int)(i & 63) * 8, h = c0 >> 7;
;         const f32x4 q0 = *(const f32x4*)(SSQG + t * 32 + h * 8);
;         const float rstd = rsqrtf(((q0.x + q0.y) + (q0.z + q0.w)) * (1.0f / 128.0f) + 1e-6f);
;         const v4u o = *(const v4u*)(Y + t * 1024 + c0), z = Z[i];
;         const f32x4 w0 = *(const f32x4*)(P.gdn_norm_w + (c0 & 127)), w1 = *(const f32x4*)(P.gdn_norm_w + (c0 & 127) + 4);
;         float y[8];
;         y[0] = bflo(o.x) * rstd * w0.x * siluf_(bflo(z.x)); y[1] = bfhi(o.x) * rstd * w0.y * siluf_(bfhi(z.x));
;         y[2] = bflo(o.y) * rstd * w0.z * siluf_(bflo(z.y)); y[3] = bfhi(o.y) * rstd * w0.w * siluf_(bfhi(z.y));
;         y[4] = bflo(o.z) * rstd * w1.x * siluf_(bflo(z.z)); y[5] = bfhi(o.z) * rstd * w1.y * siluf_(bfhi(z.z));
;         y[6] = bflo(o.w) * rstd * w1.z * siluf_(bflo(z.w)); y[7] = bfhi(o.w) * rstd * w1.w * siluf_(bfhi(z.w));
;         v4u r; r.x = pk2(y[0], y[1]); r.y = pk2(y[2], y[3]); r.z = pk2(y[4], y[5]); r.w = pk2(y[6], y[7]);
;         *(v4u*)(Y + t * 1024 + c0) = r;
	v_lshrrev_b64 v[54:55], 6, v[2:3]
	global_load_dwordx4 v[50:53], v[6:7], off
	v_lshlrev_b32_e32 v86, 1, v2
	v_lshlrev_b64 v[62:63], 7, v[54:55]
	v_and_b32_e32 v56, 0x78, v1
	v_and_b32_e32 v86, 0x60, v86
	v_lshl_add_u64 v[62:63], s[94:95], 0, v[62:63]
	v_lshlrev_b64 v[64:65], 11, v[54:55]
	v_lshlrev_b32_e32 v66, 2, v56
	v_lshl_add_u64 v[62:63], v[62:63], 0, v[86:87]
	global_load_dwordx4 v[54:57], v66, s[22:23]
	global_load_dwordx4 v[58:61], v66, s[22:23] offset:16
	v_lshl_add_u64 v[66:67], s[8:9], 0, v[64:65]
	global_load_dwordx4 v[62:65], v[62:63], off
	v_and_b32_e32 v88, 0x1f8, v1
	v_lshlrev_b32_e32 v86, 1, v88
	v_lshl_add_u64 v[70:71], v[66:67], 0, v[86:87]
	global_load_dwordx4 v[66:69], v[70:71], off
	v_lshl_add_u64 v[2:3], v[2:3], 0, s[6:7]
	v_cmp_lt_u64_e32 vcc, s[14:15], v[2:3]
	s_or_b64 s[12:13], vcc, s[12:13]
	v_lshl_add_u64 v[6:7], v[6:7], 0, s[10:11]
	v_add_u32_e32 v1, s3, v1
	s_mov_b64 s[100:101], exec
	s_mov_b64 exec, s[98:99]
	s_waitcnt vmcnt(6)
	v_lshlrev_b32_e32 v32, 16, v10
	v_mul_f32_e32 v4, 0xbfb8aa3b, v32
	v_exp_f32_e32 v4, v4
	v_lshlrev_b32_e32 v33, 16, v11
	v_lshlrev_b32_e32 v35, 16, v13
	v_lshlrev_b32_e32 v34, 16, v12
	v_and_b32_e32 v13, 0xffff0000, v13
	v_and_b32_e32 v12, 0xffff0000, v12
	v_mov_b32_e32 v36, v14
	v_mov_b32_e32 v37, v16
	v_mov_b32_e32 v16, v15
	v_mov_b32_e32 v14, v18
	v_mov_b32_e32 v15, v20
	v_mov_b32_e32 v20, v19
	v_mov_b32_e32 v18, v23
	v_mov_b32_e32 v19, v24
	v_mov_b32_e32 v23, v25
	v_pk_add_f32 v[18:19], v[18:19], v[22:23]
	v_and_b32_e32 v11, 0xffff0000, v11
	v_add_f32_e32 v18, v18, v19
	v_and_b32_e32 v10, 0xffff0000, v10
	v_mul_f32_e32 v38, 0xbfb8aa3b, v33
	v_mul_f32_e32 v40, 0xbfb8aa3b, v34
	v_mul_f32_e32 v41, 0xbfb8aa3b, v12
	v_mul_f32_e32 v42, 0xbfb8aa3b, v35
	v_mul_f32_e32 v43, 0xbfb8aa3b, v13
	v_add_f32_e32 v4, 1.0, v4
	v_fmamk_f32 v45, v18, 0x3c000000, v8
	v_mul_f32_e32 v9, 0xbfb8aa3b, v10
	v_mul_f32_e32 v39, 0xbfb8aa3b, v11
	v_exp_f32_e32 v38, v38
	v_exp_f32_e32 v40, v40
	v_exp_f32_e32 v41, v41
	v_exp_f32_e32 v42, v42
	v_exp_f32_e32 v43, v43
	v_rcp_f32_e32 v18, v4
	v_mul_f32_e32 v4, 0x4b800000, v45
	v_cmp_gt_f32_e32 vcc, s16, v45
	v_exp_f32_e32 v9, v9
	v_exp_f32_e32 v39, v39
	v_cndmask_b32_e32 v4, v45, v4, vcc
	v_rsq_f32_e32 v4, v4
	v_add_f32_e32 v19, 1.0, v38
	v_add_f32_e32 v40, 1.0, v40
	v_add_f32_e32 v41, 1.0, v41
	v_add_f32_e32 v44, 1.0, v42
	v_add_f32_e32 v43, 1.0, v43
	v_add_f32_e32 v9, 1.0, v9
	v_add_f32_e32 v39, 1.0, v39
	v_rcp_f32_e32 v19, v19
	v_rcp_f32_e32 v40, v40
	v_rcp_f32_e32 v42, v41
	v_rcp_f32_e32 v41, v44
	v_rcp_f32_e32 v43, v43
	v_rcp_f32_e32 v38, v9
	v_rcp_f32_e32 v39, v39
	v_mul_f32_e32 v9, 0x45800000, v4
	v_lshlrev_b32_e32 v23, 16, v27
	v_lshlrev_b32_e32 v22, 16, v26
	v_and_b32_e32 v25, 0xffff0000, v27
	v_and_b32_e32 v24, 0xffff0000, v26
	v_lshlrev_b32_e32 v27, 16, v29
	v_lshlrev_b32_e32 v26, 16, v28
	v_and_b32_e32 v29, 0xffff0000, v29
	v_and_b32_e32 v28, 0xffff0000, v28
	v_cndmask_b32_e32 v4, v4, v9, vcc
	v_pk_mul_f32 v[22:23], v[4:5], v[22:23] op_sel_hi:[0,1]
	v_pk_mul_f32 v[26:27], v[4:5], v[26:27] op_sel_hi:[0,1]
	v_pk_mul_f32 v[28:29], v[4:5], v[28:29] op_sel_hi:[0,1]
	v_pk_mul_f32 v[18:19], v[18:19], v[32:33]
	v_pk_mul_f32 v[32:33], v[40:41], v[34:35]
	v_pk_mul_f32 v[12:13], v[42:43], v[12:13]
	v_pk_mul_f32 v[24:25], v[4:5], v[24:25] op_sel_hi:[0,1]
	v_pk_mul_f32 v[22:23], v[36:37], v[22:23]
	v_pk_mul_f32 v[14:15], v[14:15], v[26:27]
	v_pk_mul_f32 v[20:21], v[20:21], v[28:29]
	v_pk_mul_f32 v[10:11], v[38:39], v[10:11]
	v_pk_mul_f32 v[16:17], v[16:17], v[24:25]
	v_pk_mul_f32 v[18:19], v[18:19], v[22:23]
	v_pk_mul_f32 v[14:15], v[32:33], v[14:15]
	v_pk_mul_f32 v[12:13], v[12:13], v[20:21]
	v_pk_mul_f32 v[10:11], v[10:11], v[16:17]
	v_cvt_pk_bf16_f32 v10, v18, v10
	v_cvt_pk_bf16_f32 v11, v19, v11
	v_cvt_pk_bf16_f32 v12, v14, v12
	v_cvt_pk_bf16_f32 v13, v15, v13
	global_store_dwordx4 v[30:31], v[10:13], off
	s_mov_b64 exec, s[100:101]
	s_branch .Lp4_loop
